# mixer C loop: next K fragment tails read straight into the operand registers (4 copies and a wait per tile removed)
# baseline (speedup 1.0000x reference)
.LBB0_790:
	s_addk_i32 s15, 0x1000
	s_add_i32 s14, s14, 1
	s_cmp_eq_u32 s20, s14
	s_cbranch_scc1 .LBB0_795
.LBB0_791:
	s_and_b32 s16, s15, 0x7000
	v_add_u32_e32 v114, s16, v249
	ds_read_b128 v[162:165], v114 offset:32768
	ds_read_b128 v[170:173], v114 offset:33280
	ds_read_b128 v[166:169], v114 offset:33792
	ds_read_b128 v[174:177], v114 offset:34304
	v_mfma_scale_f32_32x32x64_f8f6f4 v[114:129], v[198:203], v[186:191], v[2:17], v251, v250 op_sel_hi:[0,0,0] cbsz:2 blgp:2
	s_nop 0
	v_cvt_pknorm_u16_f32 v98, v98, v99
	v_cvt_pknorm_u16_f32 v99, v100, v101
	v_cvt_pknorm_u16_f32 v82, v82, v83
	v_cvt_pknorm_u16_f32 v83, v84, v85
	v_perm_b32 v178, v99, v98, s86
	v_perm_b32 v182, v83, v82, s86
	s_waitcnt lgkmcnt(4)
	v_mfma_scale_f32_32x32x64_f8f6f4 v[130:145], v[204:209], v[186:191], v[2:17], v251, v250 op_sel_hi:[0,0,0] cbsz:2 blgp:2
	v_cvt_pknorm_u16_f32 v82, v102, v103
	v_cvt_pknorm_u16_f32 v83, v104, v105
	v_perm_b32 v179, v83, v82, s86
	v_cvt_pknorm_u16_f32 v82, v86, v87
	v_cvt_pknorm_u16_f32 v83, v88, v89
	v_perm_b32 v183, v83, v82, s86
	s_waitcnt lgkmcnt(1)
	v_mfma_scale_f32_32x32x64_f8f6f4 v[34:49], v[146:153], v[162:169], v[34:49], v248, v248 op_sel_hi:[0,0,0]
	v_cvt_pknorm_u16_f32 v82, v106, v107
	v_cvt_pknorm_u16_f32 v83, v108, v109
	v_perm_b32 v180, v83, v82, s86
	v_cvt_pknorm_u16_f32 v82, v90, v91
	v_cvt_pknorm_u16_f32 v83, v92, v93
	v_perm_b32 v184, v83, v82, s86
	s_waitcnt lgkmcnt(0)
	v_mfma_scale_f32_32x32x64_f8f6f4 v[18:33], v[146:153], v[170:177], v[18:33], v248, v248 op_sel_hi:[0,0,0]
	v_cvt_pknorm_u16_f32 v82, v110, v111
	v_cvt_pknorm_u16_f32 v83, v112, v113
	v_perm_b32 v181, v83, v82, s86
	v_cvt_pknorm_u16_f32 v82, v94, v95
	v_cvt_pknorm_u16_f32 v83, v96, v97
	v_perm_b32 v185, v83, v82, s86
	v_mfma_scale_f32_16x16x128_f8f6f4 v[210:213], v[146:153], v[154:161], v[210:213], v248, v248 op_sel_hi:[0,0,0]
	v_mfma_scale_f32_32x32x64_f8f6f4 v[98:113], v[198:203], v[192:197], v[2:17], v251, v250 op_sel_hi:[0,0,0] cbsz:2 blgp:2
	v_mfma_scale_f32_32x32x64_f8f6f4 v[82:97], v[204:209], v[192:197], v[2:17], v251, v250 op_sel_hi:[0,0,0] cbsz:2 blgp:2
	s_nop 0
	v_cvt_pknorm_u16_f32 v114, v114, v115
	v_cvt_pknorm_u16_f32 v115, v116, v117
	v_perm_b32 v146, v115, v114, s86
	v_cvt_pknorm_u16_f32 v114, v130, v131
	v_cvt_pknorm_u16_f32 v115, v132, v133
	v_perm_b32 v150, v115, v114, s86
	v_mfma_scale_f32_32x32x64_f8f6f4 v[66:81], v[178:185], v[162:169], v[66:81], v248, v248 op_sel_hi:[0,0,0]
	s_add_i32 s4, s15, 0xffffa000
	s_and_b32 s17, s4, 0x7000
	v_add_u32_e32 v130, s17, v249
	ds_read_b128 v[198:201], v130
	ds_read_b64 v[202:203], v130 offset:1024
	ds_read_b128 v[204:207], v130 offset:512
	ds_read_b64 v[208:209], v130 offset:1536
	v_cvt_pknorm_u16_f32 v118, v118, v119
	v_cvt_pknorm_u16_f32 v119, v120, v121
	v_perm_b32 v147, v119, v118, s86
	v_cvt_pknorm_u16_f32 v118, v134, v135
	v_cvt_pknorm_u16_f32 v119, v136, v137
	v_perm_b32 v151, v119, v118, s86
	v_cvt_pknorm_u16_f32 v118, v122, v123
	v_cvt_pknorm_u16_f32 v119, v124, v125
	v_perm_b32 v148, v119, v118, s86
	v_cvt_pknorm_u16_f32 v118, v138, v139
	v_cvt_pknorm_u16_f32 v119, v140, v141
	v_perm_b32 v152, v119, v118, s86
	v_mfma_scale_f32_32x32x64_f8f6f4 v[50:65], v[178:185], v[170:177], v[50:65], v248, v248 op_sel_hi:[0,0,0]
	v_cvt_pknorm_u16_f32 v118, v126, v127
	v_cvt_pknorm_u16_f32 v119, v128, v129
	v_perm_b32 v149, v119, v118, s86
	v_cvt_pknorm_u16_f32 v118, v142, v143
	v_cvt_pknorm_u16_f32 v119, v144, v145
	v_perm_b32 v153, v119, v118, s86
	v_mfma_scale_f32_16x16x128_f8f6f4 v[214:217], v[178:185], v[154:161], v[214:217], v248, v248 op_sel_hi:[0,0,0]
	s_waitcnt vmcnt(6) lgkmcnt(0)
	s_barrier
	s_mov_b64 s[4:5], -1
	s_and_b64 vcc, exec, s[12:13]
	s_cbranch_vccz .LBB0_793
	s_add_i32 s4, s14, 8
	s_min_i32 s4, s4, s20
	s_lshl_b32 s58, s4, 6
	v_lshl_add_u64 v[118:119], v[226:227], 0, s[58:59]
	s_add_i32 s4, s16, s42
	s_mov_b32 s5, m0
	s_mov_b32 m0, s4
	s_nop 0
	global_load_lds_dwordx4 v[118:119], off
	s_mov_b32 m0, s5
	s_mov_b64 s[4:5], 0
